# baseline (speedup 1.0000x reference)
_Z11prep_tablesPKfS0_S0_S0_S0_S0_S0_S0_S0_S0_S0_S0_S0_S0_S0_S0_S0_S0_S0_PcPfPyS0_:
	s_load_dwordx2 s[24:25], s[0:1], 0xa0
	v_lshrrev_b32_e32 v1, 5, v0
	v_and_b32_e32 v36, 31, v0
	s_cmp_gt_i32 s2, 3
	s_mov_b64 s[4:5], -1
	s_cbranch_scc0 .LBB0_43
	s_load_dwordx2 s[26:27], s[0:1], 0x98
	s_load_dwordx2 s[28:29], s[0:1], 0x0
	s_cmp_gt_u32 s2, 35
	s_cbranch_scc0 .LBB0_58
	s_load_dwordx2 s[68:69], s[0:1], 0x80
	s_load_dwordx2 s[30:31], s[0:1], 0x58
	s_load_dwordx2 s[34:35], s[0:1], 0x48
	s_load_dwordx2 s[70:71], s[0:1], 0x28
	s_load_dwordx2 s[98:99], s[0:1], 0x20
	s_cmpk_gt_u32 s2, 0x53
	s_cbranch_scc0 .LBB0_39
	s_cmpk_gt_u32 s2, 0x63
	s_cbranch_scc0 .LBB0_36
	s_load_dwordx2 s[72:73], s[0:1], 0x50
	s_load_dwordx2 s[96:97], s[0:1], 0x30
	s_cmpk_lt_u32 s2, 0x68
	s_cbranch_scc0 .LBB0_33
	s_load_dwordx4 s[20:23], s[0:1], 0x60
	s_load_dwordx2 s[74:75], s[0:1], 0x88
	s_load_dwordx2 s[76:77], s[0:1], 0xb0
	s_cmpk_lg_i32 s2, 0x67
	s_cbranch_scc0 .LBB0_28
	v_lshl_or_b32 v2, s2, 6, v0
	v_add_u32_e32 v8, 0xffffe700, v2
	v_cmp_gt_u32_e32 vcc, 9, v8
	s_and_saveexec_b64 s[4:5], vcc
	s_cbranch_execz .LBB0_8
	s_load_dwordx2 s[6:7], s[0:1], 0xa8
	v_lshlrev_b32_e32 v2, 4, v8
	v_mov_b32_e32 v3, 0
	s_waitcnt lgkmcnt(0)
	v_lshl_add_u64 v[4:5], v[2:3], 3, s[6:7]
	v_mov_b32_e32 v2, v3
	global_store_dwordx2 v[4:5], v[2:3], off

.LBB0_28:
	s_and_b64 vcc, exec, s[4:5]
	s_cbranch_vccz .LBB0_32
	v_lshlrev_b32_e32 v37, 8, v0
	s_waitcnt lgkmcnt(0)
	s_load_dword s78, s[76:77], 0x0
	global_load_dwordx4 v[14:17], v37, s[68:69]
	global_load_dwordx4 v[10:13], v37, s[68:69] offset:16
	global_load_dwordx4 v[6:9], v37, s[68:69] offset:48
	global_load_dwordx4 v[2:5], v37, s[68:69] offset:32
	global_load_dwordx4 v[20:23], v37, s[68:69] offset:64
	global_load_dwordx4 v[24:27], v37, s[68:69] offset:96
	global_load_dwordx4 v[28:31], v37, s[68:69] offset:80
	global_load_dwordx4 v[32:35], v37, s[68:69] offset:112
	global_load_dwordx4 v[38:41], v37, s[68:69] offset:144
	global_load_dwordx4 v[42:45], v37, s[68:69] offset:128
	v_lshlrev_b32_e32 v18, 2, v0
	s_load_dwordx16 s[36:51], s[20:21], 0x0
	global_load_dword v70, v18, s[74:75]
	global_load_dwordx4 v[46:49], v37, s[68:69] offset:176
	global_load_dwordx4 v[50:53], v37, s[68:69] offset:160
	s_load_dwordx16 s[52:67], s[20:21], 0x40
	s_load_dwordx16 s[4:19], s[20:21], 0x80
	s_load_dwordx16 s[80:95], s[20:21], 0xc0
	global_load_dwordx4 v[54:57], v37, s[68:69] offset:224
	global_load_dwordx4 v[58:61], v37, s[68:69] offset:240
	global_load_dwordx4 v[62:65], v37, s[68:69] offset:208
	global_load_dwordx4 v[66:69], v37, s[68:69] offset:192
	s_nop 0
	global_load_dword v37, v18, s[20:21]
	global_load_dword v72, v18, s[22:23]
	v_mov_b32_e32 v19, 0
	s_mov_b32 s3, 0x8000
	s_waitcnt vmcnt(18) lgkmcnt(0)
	v_pk_mul_f32 v[16:17], v[16:17], s[38:39]
	v_pk_mul_f32 v[14:15], v[14:15], s[36:37]
	s_waitcnt vmcnt(17)
	v_pk_mul_f32 v[10:11], v[10:11], s[40:41]
	v_pk_mul_f32 v[12:13], v[12:13], s[42:43]
	s_waitcnt vmcnt(16)
	v_mul_f32_e32 v71, s48, v6
	s_waitcnt vmcnt(15)
	v_mul_f32_e32 v6, s45, v3
	s_waitcnt vmcnt(13)
	v_mul_f32_e32 v76, s60, v24
	s_waitcnt vmcnt(12)
	v_mul_f32_e32 v24, s57, v29
	v_mul_f32_e32 v73, s49, v7
	v_mul_f32_e32 v77, s61, v25
	v_pk_fma_f32 v[2:3], v[2:3], s[44:45], v[6:7] op_sel_hi:[1,1,0]
	v_pk_fma_f32 v[6:7], v[28:29], s[56:57], v[24:25] op_sel_hi:[1,1,0]
	v_pk_mov_b32 v[24:25], v[14:15], v[16:17] op_sel:[1,0]
	v_mov_b32_e32 v15, v17
	v_pk_mov_b32 v[16:17], v[10:11], v[12:13] op_sel:[1,0]
	v_mov_b32_e32 v11, v13
	v_mul_f32_e32 v74, s50, v8
	v_mul_f32_e32 v75, s51, v9
	v_pk_mul_f32 v[8:9], v[22:23], s[54:55]
	v_mul_f32_e32 v22, s47, v5
	v_pk_add_f32 v[14:15], v[24:25], v[14:15]
	v_pk_add_f32 v[10:11], v[16:17], v[10:11]
	v_pk_fma_f32 v[4:5], v[4:5], s[46:47], v[22:23] op_sel_hi:[1,1,0]
	v_add_f32_e32 v14, v14, v15
	v_pk_add_f32 v[10:11], v[10:11], v[10:11] op_sel:[0,1] op_sel_hi:[1,0]
	v_pk_mul_f32 v[20:21], v[20:21], s[52:53]
	v_mov_b32_e32 v3, v74
	v_mov_b32_e32 v5, v75
	s_waitcnt vmcnt(8)
	v_add_f32_e32 v70, v70, v14
	v_mov_b32_e32 v11, v73
	v_pk_mov_b32 v[12:13], v[20:21], v[8:9] op_sel:[1,0]
	v_mov_b32_e32 v21, v9
	v_pk_add_f32 v[2:3], v[2:3], v[4:5]
	v_pk_add_f32 v[10:11], v[70:71], v[10:11]
	v_mul_f32_e32 v78, s62, v26
	v_mul_f32_e32 v79, s63, v27
	v_pk_mul_f32 v[26:27], v[32:33], s[64:65]
	v_pk_mul_f32 v[32:33], v[34:35], s[66:67]
	v_mul_f32_e32 v35, s8, v38
	v_mul_f32_e32 v34, s59, v31
	v_pk_add_f32 v[12:13], v[12:13], v[20:21]
	v_pk_add_f32 v[2:3], v[10:11], v[2:3]
	v_pk_fma_f32 v[22:23], v[30:31], s[58:59], v[34:35] op_sel_hi:[1,1,0]
	v_pk_add_f32 v[4:5], v[12:13], v[12:13] op_sel:[0,1] op_sel_hi:[1,0]
	v_pk_add_f32 v[2:3], v[2:3], v[2:3] op_sel:[0,1] op_sel_hi:[1,0]
	v_mov_b32_e32 v7, v78
	v_mov_b32_e32 v23, v79
	v_mov_b32_e32 v5, v77
	v_mov_b32_e32 v3, v76
	v_pk_mov_b32 v[8:9], v[26:27], v[32:33] op_sel:[1,0]
	v_mov_b32_e32 v27, v33
	v_pk_add_f32 v[6:7], v[6:7], v[22:23]
	v_pk_add_f32 v[2:3], v[2:3], v[4:5]
	v_mul_f32_e32 v39, s9, v39
	v_mul_f32_e32 v80, s10, v40
	v_mul_f32_e32 v41, s11, v41
	v_mul_f32_e32 v38, s5, v43
	v_mul_f32_e32 v40, s7, v45
	v_pk_add_f32 v[8:9], v[8:9], v[26:27]
	v_pk_add_f32 v[2:3], v[2:3], v[6:7]
	v_pk_fma_f32 v[28:29], v[42:43], s[4:5], v[38:39] op_sel_hi:[1,1,0]
	v_pk_fma_f32 v[30:31], v[44:45], s[6:7], v[40:41] op_sel_hi:[1,1,0]
	v_pk_add_f32 v[8:9], v[8:9], v[8:9] op_sel:[0,1] op_sel_hi:[1,0]
	v_pk_add_f32 v[2:3], v[2:3], v[2:3] op_sel:[0,1] op_sel_hi:[1,0]
	v_mov_b32_e32 v29, v80
	v_mov_b32_e32 v31, v41
	v_mov_b32_e32 v9, v39
	v_mov_b32_e32 v3, v35
	v_pk_add_f32 v[2:3], v[2:3], v[8:9]
	v_pk_add_f32 v[4:5], v[28:29], v[30:31]
	s_waitcnt vmcnt(6)
	v_pk_mul_f32 v[6:7], v[52:53], s[14:15]
	v_pk_add_f32 v[2:3], v[2:3], v[4:5]
	v_pk_mul_f32 v[4:5], v[50:51], s[12:13]
	v_pk_add_f32 v[2:3], v[2:3], v[2:3] op_sel:[0,1] op_sel_hi:[1,0]
	v_pk_mov_b32 v[8:9], v[4:5], v[6:7] op_sel:[1,0]
	v_mov_b32_e32 v5, v7
	v_pk_add_f32 v[4:5], v[8:9], v[4:5]
	s_waitcnt vmcnt(2) lgkmcnt(0)
	v_mul_f32_e32 v6, s80, v66
	v_mul_f32_e32 v7, s81, v67
	v_pk_add_f32 v[4:5], v[4:5], v[4:5] op_sel:[0,1] op_sel_hi:[1,0]
	v_mov_b32_e32 v3, v6
	v_mov_b32_e32 v5, v7
	v_pk_add_f32 v[2:3], v[2:3], v[4:5]
	v_mul_f32_e32 v4, s17, v47
	v_mul_f32_e32 v6, s19, v49
	v_mul_f32_e32 v8, s82, v68
	v_mul_f32_e32 v9, s83, v69
	v_pk_fma_f32 v[4:5], v[46:47], s[16:17], v[4:5] op_sel_hi:[1,1,0]
	v_pk_fma_f32 v[6:7], v[48:49], s[18:19], v[6:7] op_sel_hi:[1,1,0]
	v_mov_b32_e32 v5, v8
	v_mov_b32_e32 v7, v9
	v_pk_add_f32 v[4:5], v[4:5], v[6:7]
	v_pk_mul_f32 v[6:7], v[64:65], s[86:87]
	v_pk_add_f32 v[2:3], v[2:3], v[4:5]
	v_pk_mul_f32 v[4:5], v[62:63], s[84:85]
	v_pk_add_f32 v[2:3], v[2:3], v[2:3] op_sel:[0,1] op_sel_hi:[1,0]
	v_pk_mov_b32 v[8:9], v[4:5], v[6:7] op_sel:[1,0]
	v_mov_b32_e32 v5, v7
	v_pk_add_f32 v[4:5], v[8:9], v[4:5]
	v_mul_f32_e32 v6, s92, v58
	v_mul_f32_e32 v7, s93, v59
	v_pk_add_f32 v[4:5], v[4:5], v[4:5] op_sel:[0,1] op_sel_hi:[1,0]
	v_mov_b32_e32 v3, v6
	v_mov_b32_e32 v5, v7
	v_pk_add_f32 v[2:3], v[2:3], v[4:5]
	v_mul_f32_e32 v4, s89, v55
	v_mul_f32_e32 v6, s91, v57
	v_mul_f32_e32 v8, s94, v60
	v_mul_f32_e32 v9, s95, v61
	v_pk_fma_f32 v[4:5], v[54:55], s[88:89], v[4:5] op_sel_hi:[1,1,0]
	v_pk_fma_f32 v[6:7], v[56:57], s[90:91], v[6:7] op_sel_hi:[1,1,0]
	v_mov_b32_e32 v5, v8
	v_mov_b32_e32 v7, v9
	v_pk_add_f32 v[4:5], v[4:5], v[6:7]
	s_nop 0
	v_pk_add_f32 v[2:3], v[2:3], v[4:5]
	s_nop 0
	v_add_f32_e32 v4, v2, v3
	v_lshl_add_u64 v[2:3], s[26:27], 0, v[18:19]
	v_add_co_u32_e32 v2, vcc, s3, v2
	s_nop 1
	v_addc_co_u32_e32 v3, vcc, 0, v3, vcc
	global_store_dword v[2:3], v4, off offset:2048
	s_waitcnt vmcnt(1)
	v_mul_f32_e32 v2, v37, v72
	v_cmp_eq_u32_e32 vcc, 0, v0
	s_nop 0
	v_mov_b32_dpp v2, v2 quad_perm:[1,0,3,2] row_mask:0xf bank_mask:0xf bound_ctrl:1
	v_fmac_f32_e32 v2, v37, v72
	s_nop 1
	v_add_f32_dpp v2, v2, v2 quad_perm:[2,3,0,1] row_mask:0xf bank_mask:0xf bound_ctrl:1
	s_nop 1
	v_add_f32_dpp v2, v2, v2 row_half_mirror row_mask:0xf bank_mask:0xf bound_ctrl:1
	s_nop 1
	v_add_f32_dpp v2, v2, v2 row_ror:8 row_mask:0xf bank_mask:0xf bound_ctrl:1
	v_mov_b32_e32 v3, v2
	s_nop 1
	v_permlane16_swap_b32_e32 v2, v3
	v_add_f32_e32 v2, v2, v3
	v_mov_b32_e32 v3, v2
	s_nop 1
	v_permlane32_swap_b32_e32 v2, v3
	s_and_saveexec_b64 s[4:5], vcc
	s_cbranch_execz .LBB0_31
	v_add_f32_e32 v2, v2, v3
	v_mov_b32_e32 v3, 0x4000
	s_waitcnt lgkmcnt(0)
	v_add_f32_e32 v2, s78, v2
	global_store_dword v3, v2, s[24:25]

.LBB0_33:
	s_andn2_b64 vcc, exec, s[4:5]
	s_cbranch_vccnz .LBB0_35
	v_lshl_or_b32 v2, s2, 6, v0
	v_add_u32_e32 v4, 0xffffe600, v2
	v_mov_b32_e32 v5, 0
	v_lshlrev_b64 v[2:3], 2, v[4:5]
	v_lshlrev_b32_e32 v4, 6, v4
	s_waitcnt lgkmcnt(0)
	v_lshl_add_u64 v[66:67], v[4:5], 2, s[70:71]
	global_load_dwordx4 v[4:7], v[66:67], off
	global_load_dwordx4 v[8:11], v[66:67], off offset:16
	global_load_dwordx4 v[12:15], v[66:67], off offset:48
	global_load_dwordx4 v[16:19], v[66:67], off offset:32
	global_load_dwordx4 v[20:23], v[66:67], off offset:64
	global_load_dwordx4 v[24:27], v[66:67], off offset:96
	global_load_dwordx4 v[28:31], v[66:67], off offset:80
	global_load_dwordx4 v[32:35], v[66:67], off offset:112
	global_load_dwordx4 v[38:41], v[66:67], off offset:144
	global_load_dwordx4 v[42:45], v[66:67], off offset:128
	v_lshl_add_u64 v[50:51], s[96:97], 0, v[2:3]
	global_load_dword v37, v[50:51], off
	global_load_dwordx4 v[46:49], v[66:67], off offset:160
	s_load_dwordx16 s[52:67], s[72:73], 0x0
	s_load_dwordx16 s[36:51], s[72:73], 0x40
	s_load_dwordx16 s[4:19], s[72:73], 0x80
	s_load_dwordx16 s[80:95], s[72:73], 0xc0
	global_load_dwordx4 v[50:53], v[66:67], off offset:176
	global_load_dwordx4 v[54:57], v[66:67], off offset:208
	global_load_dwordx4 v[58:61], v[66:67], off offset:192
	global_load_dwordx4 v[62:65], v[66:67], off offset:224
	s_nop 0
	global_load_dwordx4 v[66:69], v[66:67], off offset:240
	v_lshl_add_u64 v[2:3], s[26:27], 0, v[2:3]
	v_add_co_u32_e32 v2, vcc, 0x8000, v2
	s_waitcnt vmcnt(16) lgkmcnt(0)
	v_pk_mul_f32 v[6:7], v[6:7], s[54:55]
	v_pk_mul_f32 v[4:5], v[4:5], s[52:53]
	s_waitcnt vmcnt(15)
	v_pk_mul_f32 v[10:11], v[10:11], s[58:59]
	v_pk_mul_f32 v[8:9], v[8:9], s[56:57]
	s_waitcnt vmcnt(14)
	v_mul_f32_e32 v71, s64, v12
	s_waitcnt vmcnt(13)
	v_mul_f32_e32 v12, s61, v17
	s_waitcnt vmcnt(11)
	v_mul_f32_e32 v74, s44, v24
	s_waitcnt vmcnt(10)
	v_mul_f32_e32 v24, s41, v29
	v_mul_f32_e32 v72, s65, v13
	v_pk_mul_f32 v[22:23], v[22:23], s[38:39]
	v_pk_mul_f32 v[20:21], v[20:21], s[36:37]
	v_mul_f32_e32 v75, s45, v25
	v_pk_fma_f32 v[12:13], v[16:17], s[60:61], v[12:13] op_sel_hi:[1,1,0]
	v_pk_fma_f32 v[16:17], v[28:29], s[40:41], v[24:25] op_sel_hi:[1,1,0]
	v_pk_mov_b32 v[24:25], v[4:5], v[6:7] op_sel:[1,0]
	v_mov_b32_e32 v5, v7
	v_pk_mov_b32 v[6:7], v[8:9], v[10:11] op_sel:[1,0]
	v_mov_b32_e32 v9, v11
	v_mul_f32_e32 v70, s66, v14
	v_mul_f32_e32 v14, s63, v19
	v_pk_mov_b32 v[10:11], v[20:21], v[22:23] op_sel:[1,0]
	v_mov_b32_e32 v21, v23
	v_pk_add_f32 v[4:5], v[24:25], v[4:5]
	v_pk_add_f32 v[6:7], v[6:7], v[8:9]
	v_mul_f32_e32 v73, s67, v15
	v_pk_fma_f32 v[14:15], v[18:19], s[62:63], v[14:15] op_sel_hi:[1,1,0]
	v_pk_add_f32 v[8:9], v[10:11], v[20:21]
	v_add_f32_e32 v20, v4, v5
	v_pk_add_f32 v[4:5], v[6:7], v[6:7] op_sel:[0,1] op_sel_hi:[1,0]
	v_mov_b32_e32 v13, v70
	v_mov_b32_e32 v15, v73
	s_waitcnt vmcnt(6)
	v_add_f32_e32 v70, v37, v20
	v_mov_b32_e32 v5, v72
	v_pk_add_f32 v[6:7], v[12:13], v[14:15]
	v_pk_add_f32 v[4:5], v[70:71], v[4:5]
	v_mul_f32_e32 v76, s46, v26
	v_mul_f32_e32 v26, s43, v31
	v_pk_add_f32 v[4:5], v[4:5], v[6:7]
	v_mul_f32_e32 v77, s47, v27
	v_pk_fma_f32 v[18:19], v[30:31], s[42:43], v[26:27] op_sel_hi:[1,1,0]
	v_pk_add_f32 v[8:9], v[8:9], v[8:9] op_sel:[0,1] op_sel_hi:[1,0]
	v_pk_add_f32 v[4:5], v[4:5], v[4:5] op_sel:[0,1] op_sel_hi:[1,0]
	v_pk_mul_f32 v[34:35], v[34:35], s[50:51]
	v_pk_mul_f32 v[32:33], v[32:33], s[48:49]
	v_mov_b32_e32 v17, v76
	v_mov_b32_e32 v19, v77
	v_mov_b32_e32 v9, v75
	v_mov_b32_e32 v5, v74
	v_pk_mov_b32 v[22:23], v[32:33], v[34:35] op_sel:[1,0]
	v_mov_b32_e32 v33, v35
	v_pk_add_f32 v[12:13], v[16:17], v[18:19]
	v_pk_add_f32 v[4:5], v[4:5], v[8:9]
	v_mul_f32_e32 v78, s8, v38
	v_mul_f32_e32 v39, s9, v39
	v_mul_f32_e32 v79, s10, v40
	v_mul_f32_e32 v41, s11, v41
	v_mul_f32_e32 v38, s5, v43
	v_mul_f32_e32 v40, s7, v45
	v_pk_add_f32 v[10:11], v[22:23], v[32:33]
	v_pk_add_f32 v[4:5], v[4:5], v[12:13]
	v_pk_fma_f32 v[26:27], v[42:43], s[4:5], v[38:39] op_sel_hi:[1,1,0]
	v_pk_fma_f32 v[28:29], v[44:45], s[6:7], v[40:41] op_sel_hi:[1,1,0]
	v_pk_add_f32 v[10:11], v[10:11], v[10:11] op_sel:[0,1] op_sel_hi:[1,0]
	v_pk_add_f32 v[4:5], v[4:5], v[4:5] op_sel:[0,1] op_sel_hi:[1,0]
	v_mov_b32_e32 v27, v79
	v_mov_b32_e32 v29, v41
	v_mov_b32_e32 v11, v39
	v_mov_b32_e32 v5, v78
	s_waitcnt vmcnt(5)
	v_pk_mul_f32 v[6:7], v[48:49], s[14:15]
	v_pk_mul_f32 v[8:9], v[46:47], s[12:13]
	v_pk_add_f32 v[14:15], v[26:27], v[28:29]
	v_pk_add_f32 v[4:5], v[4:5], v[10:11]
	v_pk_mov_b32 v[10:11], v[8:9], v[6:7] op_sel:[1,0]
	v_mov_b32_e32 v9, v7
	v_pk_add_f32 v[4:5], v[4:5], v[14:15]
	v_pk_add_f32 v[6:7], v[10:11], v[8:9]
	s_waitcnt vmcnt(2) lgkmcnt(0)
	v_mul_f32_e32 v8, s80, v58
	v_mul_f32_e32 v9, s81, v59
	v_pk_add_f32 v[4:5], v[4:5], v[4:5] op_sel:[0,1] op_sel_hi:[1,0]
	v_pk_add_f32 v[6:7], v[6:7], v[6:7] op_sel:[0,1] op_sel_hi:[1,0]
	v_mov_b32_e32 v5, v8
	v_mov_b32_e32 v7, v9
	v_pk_add_f32 v[4:5], v[4:5], v[6:7]
	v_mul_f32_e32 v6, s17, v51
	v_mul_f32_e32 v8, s19, v53
	v_mul_f32_e32 v10, s82, v60
	v_mul_f32_e32 v11, s83, v61
	v_pk_fma_f32 v[6:7], v[50:51], s[16:17], v[6:7] op_sel_hi:[1,1,0]
	v_pk_fma_f32 v[8:9], v[52:53], s[18:19], v[8:9] op_sel_hi:[1,1,0]
	v_mov_b32_e32 v7, v10
	v_mov_b32_e32 v9, v11
	v_pk_add_f32 v[6:7], v[6:7], v[8:9]
	v_pk_mul_f32 v[8:9], v[54:55], s[84:85]
	v_pk_add_f32 v[4:5], v[4:5], v[6:7]
	v_pk_mul_f32 v[6:7], v[56:57], s[86:87]
	v_pk_add_f32 v[4:5], v[4:5], v[4:5] op_sel:[0,1] op_sel_hi:[1,0]
	v_pk_mov_b32 v[10:11], v[8:9], v[6:7] op_sel:[1,0]
	v_mov_b32_e32 v9, v7
	v_pk_add_f32 v[6:7], v[10:11], v[8:9]
	s_waitcnt vmcnt(0)
	v_mul_f32_e32 v8, s92, v66
	v_mul_f32_e32 v9, s93, v67
	v_pk_add_f32 v[6:7], v[6:7], v[6:7] op_sel:[0,1] op_sel_hi:[1,0]
	v_mov_b32_e32 v5, v8
	v_mov_b32_e32 v7, v9
	v_pk_add_f32 v[4:5], v[4:5], v[6:7]
	v_mul_f32_e32 v6, s89, v63
	v_mul_f32_e32 v8, s91, v65
	v_mul_f32_e32 v10, s94, v68
	v_mul_f32_e32 v11, s95, v69
	v_pk_fma_f32 v[6:7], v[62:63], s[88:89], v[6:7] op_sel_hi:[1,1,0]
	v_pk_fma_f32 v[8:9], v[64:65], s[90:91], v[8:9] op_sel_hi:[1,1,0]
	v_mov_b32_e32 v7, v10
	v_mov_b32_e32 v9, v11
	v_pk_add_f32 v[6:7], v[6:7], v[8:9]
	v_addc_co_u32_e32 v3, vcc, 0, v3, vcc
	v_pk_add_f32 v[4:5], v[4:5], v[6:7]
	s_nop 0
	v_add_f32_e32 v4, v4, v5
	global_store_dword v[2:3], v4, off

.LBB0_36:
	s_andn2_b64 vcc, exec, s[4:5]
	s_cbranch_vccnz .LBB0_38
	s_add_i32 s3, s2, 0xffffffac
	s_lshl_b32 s4, s3, 3
	v_and_or_b32 v2, s4, 32, v36
	v_lshlrev_b32_e32 v34, 8, v2
	s_waitcnt lgkmcnt(0)
	global_load_dwordx4 v[14:17], v34, s[28:29]
	global_load_dwordx4 v[10:13], v34, s[28:29] offset:16
	global_load_dwordx4 v[6:9], v34, s[28:29] offset:32
	global_load_dwordx4 v[2:5], v34, s[28:29] offset:48
	global_load_dwordx4 v[30:33], v34, s[28:29] offset:64
	global_load_dwordx4 v[26:29], v34, s[28:29] offset:80
	global_load_dwordx4 v[22:25], v34, s[28:29] offset:96
	global_load_dwordx4 v[18:21], v34, s[28:29] offset:112
	global_load_dwordx4 v[38:41], v34, s[28:29] offset:128
	global_load_dwordx4 v[42:45], v34, s[28:29] offset:144
	global_load_dwordx4 v[46:49], v34, s[28:29] offset:176
	global_load_dwordx4 v[50:53], v34, s[28:29] offset:160
	global_load_dwordx4 v[54:57], v34, s[28:29] offset:240
	global_load_dwordx4 v[58:61], v34, s[28:29] offset:224
	global_load_dwordx4 v[62:65], v34, s[28:29] offset:208
	global_load_dwordx4 v[66:69], v34, s[28:29] offset:192
	s_lshl_b32 s4, s2, 3
	s_lshl_b32 s5, s3, 2
	s_and_b32 s4, s4, 24
	v_mov_b32_e32 v35, 0
	v_lshl_or_b32 v37, v1, 2, s4
	s_and_b32 s4, s5, 0x7fffffe0
	v_lshl_add_u64 v[70:71], s[28:29], 0, v[34:35]
	v_or_b32_e32 v34, s4, v37
	v_lshlrev_b64 v[72:73], 2, v[34:35]
	v_lshl_add_u64 v[70:71], v[70:71], 0, v[72:73]
	s_waitcnt lgkmcnt(0)
	v_lshl_add_u64 v[74:75], s[98:99], 0, v[72:73]
	s_load_dwordx16 s[52:67], s[98:99], 0x0
	s_load_dwordx16 s[36:51], s[98:99], 0x40
	s_load_dwordx16 s[4:19], s[98:99], 0x80
	s_load_dwordx16 s[80:95], s[98:99], 0xc0
	global_load_dwordx4 v[70:73], v[70:71], off
	s_nop 0
	global_load_dwordx4 v[74:77], v[74:75], off
	s_waitcnt vmcnt(17) lgkmcnt(0)
	v_pk_add_f32 v[16:17], v[16:17], s[54:55]
	v_pk_add_f32 v[14:15], v[14:15], s[52:53]
	s_waitcnt vmcnt(16)
	v_pk_add_f32 v[10:11], v[10:11], s[56:57]
	v_pk_add_f32 v[12:13], v[12:13], s[58:59]
	v_pk_mov_b32 v[78:79], v[14:15], v[16:17] op_sel:[1,0]
	v_mov_b32_e32 v15, v17
	v_pk_mov_b32 v[16:17], v[10:11], v[12:13] op_sel:[1,0]
	v_mov_b32_e32 v11, v13
	v_pk_add_f32 v[14:15], v[78:79], v[14:15]
	v_pk_add_f32 v[10:11], v[16:17], v[10:11]
	s_waitcnt vmcnt(15)
	v_pk_add_f32 v[8:9], v[8:9], s[62:63]
	v_pk_add_f32 v[6:7], v[6:7], s[60:61]
	s_waitcnt vmcnt(14)
	v_pk_add_f32 v[4:5], v[4:5], s[66:67]
	v_pk_add_f32 v[2:3], v[2:3], s[64:65]
	s_waitcnt vmcnt(12)
	v_pk_add_f32 v[26:27], v[26:27], s[40:41]
	s_waitcnt vmcnt(11)
	v_pk_add_f32 v[24:25], v[24:25], s[46:47]
	s_waitcnt vmcnt(10)
	v_pk_add_f32 v[18:19], v[18:19], s[48:49]
	v_pk_add_f32 v[20:21], v[20:21], s[50:51]
	v_add_f32_e32 v14, v14, v15
	v_pk_add_f32 v[10:11], v[10:11], v[10:11] op_sel:[0,1] op_sel_hi:[1,0]
	v_pk_add_f32 v[32:33], v[32:33], s[38:39]
	v_pk_add_f32 v[30:31], v[30:31], s[36:37]
	v_add_f32_e32 v6, v6, v7
	v_add_f32_e32 v8, v8, v9
	v_mov_b32_e32 v7, v4
	v_mov_b32_e32 v9, v5
	v_add_f32_e32 v12, v26, v27
	v_mov_b32_e32 v13, v24
	v_mov_b32_e32 v27, v25
	v_pk_mov_b32 v[24:25], v[18:19], v[20:21] op_sel:[1,0]
	v_mov_b32_e32 v19, v21
	v_mov_b32_e32 v21, v2
	v_add_f32_e32 v20, 0, v14
	v_mov_b32_e32 v11, v3
	v_pk_mov_b32 v[4:5], v[30:31], v[32:33] op_sel:[1,0]
	v_mov_b32_e32 v31, v33
	v_pk_add_f32 v[6:7], v[6:7], v[8:9]
	v_pk_add_f32 v[10:11], v[20:21], v[10:11]
	v_pk_add_f32 v[4:5], v[4:5], v[30:31]
	v_pk_add_f32 v[6:7], v[10:11], v[6:7]
	v_pk_add_f32 v[28:29], v[28:29], s[42:43]
	v_pk_add_f32 v[22:23], v[22:23], s[44:45]
	v_pk_add_f32 v[4:5], v[4:5], v[4:5] op_sel:[0,1] op_sel_hi:[1,0]
	v_pk_add_f32 v[6:7], v[6:7], v[6:7] op_sel:[0,1] op_sel_hi:[1,0]
	v_add_f32_e32 v26, v28, v29
	v_mov_b32_e32 v5, v23
	v_mov_b32_e32 v7, v22
	v_pk_add_f32 v[8:9], v[12:13], v[26:27]
	v_pk_add_f32 v[4:5], v[6:7], v[4:5]
	v_pk_add_f32 v[12:13], v[24:25], v[18:19]
	v_pk_add_f32 v[4:5], v[4:5], v[8:9]
	s_waitcnt vmcnt(9)
	v_pk_add_f32 v[40:41], v[40:41], s[6:7]
	v_pk_add_f32 v[38:39], v[38:39], s[4:5]
	s_waitcnt vmcnt(8)
	v_pk_add_f32 v[44:45], v[44:45], s[10:11]
	v_pk_add_f32 v[42:43], v[42:43], s[8:9]
	v_pk_add_f32 v[12:13], v[12:13], v[12:13] op_sel:[0,1] op_sel_hi:[1,0]
	v_pk_add_f32 v[4:5], v[4:5], v[4:5] op_sel:[0,1] op_sel_hi:[1,0]
	v_add_f32_e32 v2, v38, v39
	v_add_f32_e32 v28, v40, v41
	v_mov_b32_e32 v5, v42
	v_mov_b32_e32 v13, v43
	v_mov_b32_e32 v3, v44
	v_mov_b32_e32 v29, v45
	v_pk_add_f32 v[4:5], v[4:5], v[12:13]
	v_pk_add_f32 v[2:3], v[2:3], v[28:29]
	s_waitcnt vmcnt(6)
	v_pk_add_f32 v[6:7], v[52:53], s[14:15]
	v_pk_add_f32 v[2:3], v[4:5], v[2:3]
	v_pk_add_f32 v[4:5], v[50:51], s[12:13]
	v_pk_add_f32 v[2:3], v[2:3], v[2:3] op_sel:[0,1] op_sel_hi:[1,0]
	v_pk_mov_b32 v[8:9], v[4:5], v[6:7] op_sel:[1,0]
	v_mov_b32_e32 v5, v7
	v_pk_add_f32 v[4:5], v[8:9], v[4:5]
	v_pk_add_f32 v[6:7], v[48:49], s[18:19]
	v_pk_add_f32 v[4:5], v[4:5], v[4:5] op_sel:[0,1] op_sel_hi:[1,0]
	v_pk_add_f32 v[8:9], v[46:47], s[16:17]
	s_waitcnt vmcnt(2) lgkmcnt(0)
	v_pk_add_f32 v[10:11], v[68:69], s[82:83]
	v_pk_add_f32 v[12:13], v[66:67], s[80:81]
	v_add_f32_e32 v8, v8, v9
	v_add_f32_e32 v6, v6, v7
	v_mov_b32_e32 v3, v12
	v_mov_b32_e32 v5, v13
	v_mov_b32_e32 v9, v10
	v_mov_b32_e32 v7, v11
	v_pk_add_f32 v[2:3], v[2:3], v[4:5]
	v_pk_add_f32 v[4:5], v[8:9], v[6:7]
	v_pk_add_f32 v[6:7], v[64:65], s[86:87]
	v_pk_add_f32 v[2:3], v[2:3], v[4:5]
	v_pk_add_f32 v[4:5], v[62:63], s[84:85]
	v_pk_add_f32 v[2:3], v[2:3], v[2:3] op_sel:[0,1] op_sel_hi:[1,0]
	v_pk_mov_b32 v[8:9], v[4:5], v[6:7] op_sel:[1,0]
	v_mov_b32_e32 v5, v7
	v_pk_add_f32 v[4:5], v[8:9], v[4:5]
	v_pk_add_f32 v[6:7], v[60:61], s[90:91]
	v_pk_add_f32 v[4:5], v[4:5], v[4:5] op_sel:[0,1] op_sel_hi:[1,0]
	v_pk_add_f32 v[8:9], v[58:59], s[88:89]
	v_pk_add_f32 v[10:11], v[56:57], s[94:95]
	v_pk_add_f32 v[12:13], v[54:55], s[92:93]
	v_add_f32_e32 v8, v8, v9
	v_add_f32_e32 v6, v6, v7
	v_mov_b32_e32 v3, v12
	v_mov_b32_e32 v5, v13
	v_mov_b32_e32 v9, v10
	v_mov_b32_e32 v7, v11
	v_pk_add_f32 v[2:3], v[2:3], v[4:5]
	v_pk_add_f32 v[4:5], v[8:9], v[6:7]
	s_nop 0
	v_pk_add_f32 v[2:3], v[2:3], v[4:5]
	s_waitcnt vmcnt(0)
	v_pk_add_f32 v[4:5], v[72:73], v[76:77]
	v_add_f32_e32 v6, v2, v3
	v_pk_add_f32 v[2:3], v[70:71], v[74:75]
	v_fmamk_f32 v5, v6, 0xbc800000, v5
	v_fmac_f32_e32 v4, 0xbc800000, v6
	v_fmamk_f32 v3, v6, 0xbc800000, v3
	v_fmac_f32_e32 v2, 0xbc800000, v6
	v_lshlrev_b32_e32 v6, 4, v0
	v_lshl_or_b32 v34, s3, 10, v6
	v_lshl_add_u64 v[6:7], s[26:27], 0, v[34:35]
	v_add_co_u32_e32 v6, vcc, 0x8000, v6
	s_nop 1
	v_addc_co_u32_e32 v7, vcc, 0, v7, vcc
	global_store_dwordx4 v[6:7], v[2:5], off offset:3072

	.amdhsa_kernel _Z11prep_tablesPKfS0_S0_S0_S0_S0_S0_S0_S0_S0_S0_S0_S0_S0_S0_S0_S0_S0_S0_PcPfPyS0_
		.amdhsa_group_segment_fixed_size 0
		.amdhsa_private_segment_fixed_size 0
		.amdhsa_kernarg_size 184
		.amdhsa_user_sgpr_count 2
		.amdhsa_user_sgpr_dispatch_ptr 0
		.amdhsa_user_sgpr_queue_ptr 0
		.amdhsa_user_sgpr_kernarg_segment_ptr 1
		.amdhsa_user_sgpr_dispatch_id 0
		.amdhsa_user_sgpr_kernarg_preload_length 0
		.amdhsa_user_sgpr_kernarg_preload_offset 0
		.amdhsa_user_sgpr_private_segment_size 0
		.amdhsa_uses_dynamic_stack 0
		.amdhsa_enable_private_segment 0
		.amdhsa_system_sgpr_workgroup_id_x 1
		.amdhsa_system_sgpr_workgroup_id_y 0
		.amdhsa_system_sgpr_workgroup_id_z 0
		.amdhsa_system_sgpr_workgroup_info 0
		.amdhsa_system_vgpr_workitem_id 0
		.amdhsa_next_free_vgpr 100
		.amdhsa_next_free_sgpr 100
		.amdhsa_accum_offset 84
		.amdhsa_reserve_vcc 1
		.amdhsa_float_round_mode_32 0
		.amdhsa_float_round_mode_16_64 0
		.amdhsa_float_denorm_mode_32 3
		.amdhsa_float_denorm_mode_16_64 3
		.amdhsa_dx10_clamp 1
		.amdhsa_ieee_mode 1
		.amdhsa_fp16_overflow 0
		.amdhsa_tg_split 0
		.amdhsa_exception_fp_ieee_invalid_op 0
		.amdhsa_exception_fp_denorm_src 0
		.amdhsa_exception_fp_ieee_div_zero 0
		.amdhsa_exception_fp_ieee_overflow 0
		.amdhsa_exception_fp_ieee_underflow 0
		.amdhsa_exception_fp_ieee_inexact 0
		.amdhsa_exception_int_div_zero 0
	.end_amdhsa_kernel

amdhsa.kernels:
  - .agpr_count:     16
    .args:
      - .actual_access:  read_only
        .address_space:  global
        .offset:         0
        .size:           8
        .value_kind:     global_buffer
      - .actual_access:  read_only
        .address_space:  global
        .offset:         8
        .size:           8
        .value_kind:     global_buffer
      - .actual_access:  read_only
        .address_space:  global
        .offset:         16
        .size:           8
        .value_kind:     global_buffer
      - .actual_access:  read_only
        .address_space:  global
        .offset:         24
        .size:           8
        .value_kind:     global_buffer
      - .actual_access:  read_only
        .address_space:  global
        .offset:         32
        .size:           8
        .value_kind:     global_buffer
      - .actual_access:  read_only
        .address_space:  global
        .offset:         40
        .size:           8
        .value_kind:     global_buffer
      - .actual_access:  read_only
        .address_space:  global
        .offset:         48
        .size:           8
        .value_kind:     global_buffer
      - .actual_access:  read_only
        .address_space:  global
        .offset:         56
        .size:           8
        .value_kind:     global_buffer
      - .actual_access:  read_only
        .address_space:  global
        .offset:         64
        .size:           8
        .value_kind:     global_buffer
      - .actual_access:  read_only
        .address_space:  global
        .offset:         72
        .size:           8
        .value_kind:     global_buffer
      - .actual_access:  read_only
        .address_space:  global
        .offset:         80
        .size:           8
        .value_kind:     global_buffer
      - .actual_access:  read_only
        .address_space:  global
        .offset:         88
        .size:           8
        .value_kind:     global_buffer
      - .actual_access:  read_only
        .address_space:  global
        .offset:         96
        .size:           8
        .value_kind:     global_buffer
      - .actual_access:  read_only
        .address_space:  global
        .offset:         104
        .size:           8
        .value_kind:     global_buffer
      - .actual_access:  read_only
        .address_space:  global
        .offset:         112
        .size:           8
        .value_kind:     global_buffer
      - .actual_access:  read_only
        .address_space:  global
        .offset:         120
        .size:           8
        .value_kind:     global_buffer
      - .actual_access:  read_only
        .address_space:  global
        .offset:         128
        .size:           8
        .value_kind:     global_buffer
      - .actual_access:  read_only
        .address_space:  global
        .offset:         136
        .size:           8
        .value_kind:     global_buffer
      - .actual_access:  read_only
        .address_space:  global
        .offset:         144
        .size:           8
        .value_kind:     global_buffer
      - .actual_access:  write_only
        .address_space:  global
        .offset:         152
        .size:           8
        .value_kind:     global_buffer
      - .actual_access:  write_only
        .address_space:  global
        .offset:         160
        .size:           8
        .value_kind:     global_buffer
      - .actual_access:  write_only
        .address_space:  global
        .offset:         168
        .size:           8
        .value_kind:     global_buffer
      - .actual_access:  read_only
        .address_space:  global
        .offset:         176
        .size:           8
        .value_kind:     global_buffer
    .group_segment_fixed_size: 0
    .kernarg_segment_align: 8
    .kernarg_segment_size: 184
    .language:       OpenCL C
    .language_version:
      - 2
      - 0
    .max_flat_workgroup_size: 64
    .name:           _Z11prep_tablesPKfS0_S0_S0_S0_S0_S0_S0_S0_S0_S0_S0_S0_S0_S0_S0_S0_S0_S0_PcPfPyS0_
    .private_segment_fixed_size: 0
    .sgpr_count:     106
    .sgpr_spill_count: 0
    .symbol:         _Z11prep_tablesPKfS0_S0_S0_S0_S0_S0_S0_S0_S0_S0_S0_S0_S0_S0_S0_S0_S0_S0_PcPfPyS0_.kd
    .uniform_work_group_size: 1
    .uses_dynamic_stack: false
    .vgpr_count:     100
    .vgpr_spill_count: 0
    .wavefront_size: 64
  - .agpr_count:     0
    .args:
      - .actual_access:  read_only
        .address_space:  global
        .offset:         0
        .size:           8
        .value_kind:     global_buffer
      - .actual_access:  read_only
        .address_space:  global
        .offset:         8
        .size:           8
        .value_kind:     global_buffer
      - .actual_access:  read_only
        .address_space:  global
        .offset:         16
        .size:           8
        .value_kind:     global_buffer
      - .actual_access:  read_only
        .address_space:  global
        .offset:         24
        .size:           8
        .value_kind:     global_buffer
      - .address_space:  global
        .offset:         32
        .size:           8
        .value_kind:     global_buffer
      - .actual_access:  read_only
        .address_space:  global
        .offset:         40
        .size:           8
        .value_kind:     global_buffer
      - .actual_access:  read_only
        .address_space:  global
        .offset:         48
        .size:           8
        .value_kind:     global_buffer
      - .actual_access:  read_only
        .address_space:  global
        .offset:         56
        .size:           8
        .value_kind:     global_buffer
      - .actual_access:  read_only
        .address_space:  global
        .offset:         64
        .size:           8
        .value_kind:     global_buffer
      - .address_space:  global
        .offset:         72
        .size:           8
        .value_kind:     global_buffer
      - .actual_access:  write_only
        .address_space:  global
        .offset:         80
        .size:           8
        .value_kind:     global_buffer
    .group_segment_fixed_size: 150528
    .kernarg_segment_align: 8
    .kernarg_segment_size: 88
    .language:       OpenCL C
    .language_version:
      - 2
      - 0
    .max_flat_workgroup_size: 512
    .name:           _Z9fast_mainILb0EEvPKiS1_S1_PKfPKcS3_PfS6_PiPyS6_
    .private_segment_fixed_size: 0
    .sgpr_count:     22
    .sgpr_spill_count: 0
    .symbol:         _Z9fast_mainILb0EEvPKiS1_S1_PKfPKcS3_PfS6_PiPyS6_.kd
    .uniform_work_group_size: 1
    .uses_dynamic_stack: false
    .vgpr_count:     216
    .vgpr_spill_count: 0
    .wavefront_size: 64
